# fused router partials in out-proj epilogue + parallel (ballot/mbcnt) expert-list insertion in the router phase
# speedup vs baseline: 1.0352x; 1.0157x over previous
; __global__ void __launch_bounds__(512, 2) hymba_fwd(Args args) {
;     ...
;             if (wave == 0 && lane < NEXP) {
;                 const int e = lane; int cnt = 0;
;                 for (int i = 0; i < 64; ++i) cnt += (selE[i] == e) ? 1 : 0;
;                 unsigned base = 0u;
;                 if (cnt) base = __hip_atomic_fetch_add((unsigned*)(ctl + CW_CNT + 64 * e), (unsigned)cnt, RLX_AGENT);
;                 for (int i = 0; i < 64; ++i) if (selE[i] == e) { const int t = t0 + (i >> 1); ltok[e * SEQ + base] = t; lw[e * SEQ + base] = selW[i]; tokpos[2 * t + (i & 1)] = (e << 16) | (int)base; ++base; }
.LBB0_604:
	s_or_b64 exec, exec, s[20:21]
	s_waitcnt lgkmcnt(0)
	s_barrier
	s_mov_b64 s[12:13], exec
	s_cmp_lg_u32 s92, 0
	s_cbranch_scc1 .LBB0_552
	v_lshlrev_b32_e32 v1, 2, v153
	ds_read_b32 v2, v1 offset:56448
	ds_read_b32 v3, v1 offset:56704
	v_mov_b32_e32 v4, 0
	v_mov_b32_e32 v5, 0
	s_waitcnt lgkmcnt(0)
	v_cmp_eq_u32_e64 s[20:21], 0, v2
	s_nop 1
	v_mbcnt_lo_u32_b32 v6, s20, 0
	v_mbcnt_hi_u32_b32 v6, s21, v6
	s_bcnt1_i32_b64 s16, s[20:21]
	v_cndmask_b32_e64 v4, v4, v6, s[20:21]
	v_writelane_b32 v5, s16, 0
	v_cmp_eq_u32_e64 s[20:21], 1, v2
	s_nop 1
	v_mbcnt_lo_u32_b32 v6, s20, 0
	v_mbcnt_hi_u32_b32 v6, s21, v6
	s_bcnt1_i32_b64 s16, s[20:21]
	v_cndmask_b32_e64 v4, v4, v6, s[20:21]
	v_writelane_b32 v5, s16, 1
	v_cmp_eq_u32_e64 s[20:21], 2, v2
	s_nop 1
	v_mbcnt_lo_u32_b32 v6, s20, 0
	v_mbcnt_hi_u32_b32 v6, s21, v6
	s_bcnt1_i32_b64 s16, s[20:21]
	v_cndmask_b32_e64 v4, v4, v6, s[20:21]
	v_writelane_b32 v5, s16, 2
	v_cmp_eq_u32_e64 s[20:21], 3, v2
	s_nop 1
	v_mbcnt_lo_u32_b32 v6, s20, 0
	v_mbcnt_hi_u32_b32 v6, s21, v6
	s_bcnt1_i32_b64 s16, s[20:21]
	v_cndmask_b32_e64 v4, v4, v6, s[20:21]
	v_writelane_b32 v5, s16, 3
	v_cmp_eq_u32_e64 s[20:21], 4, v2
	s_nop 1
	v_mbcnt_lo_u32_b32 v6, s20, 0
	v_mbcnt_hi_u32_b32 v6, s21, v6
	s_bcnt1_i32_b64 s16, s[20:21]
	v_cndmask_b32_e64 v4, v4, v6, s[20:21]
	v_writelane_b32 v5, s16, 4
	v_cmp_eq_u32_e64 s[20:21], 5, v2
	s_nop 1
	v_mbcnt_lo_u32_b32 v6, s20, 0
	v_mbcnt_hi_u32_b32 v6, s21, v6
	s_bcnt1_i32_b64 s16, s[20:21]
	v_cndmask_b32_e64 v4, v4, v6, s[20:21]
	v_writelane_b32 v5, s16, 5
	v_cmp_eq_u32_e64 s[20:21], 6, v2
	s_nop 1
	v_mbcnt_lo_u32_b32 v6, s20, 0
	v_mbcnt_hi_u32_b32 v6, s21, v6
	s_bcnt1_i32_b64 s16, s[20:21]
	v_cndmask_b32_e64 v4, v4, v6, s[20:21]
	v_writelane_b32 v5, s16, 6
	v_cmp_eq_u32_e64 s[20:21], 7, v2
	s_nop 1
	v_mbcnt_lo_u32_b32 v6, s20, 0
	v_mbcnt_hi_u32_b32 v6, s21, v6
	s_bcnt1_i32_b64 s16, s[20:21]
	v_cndmask_b32_e64 v4, v4, v6, s[20:21]
	v_writelane_b32 v5, s16, 7
	v_cmp_eq_u32_e64 s[20:21], 8, v2
	s_nop 1
	v_mbcnt_lo_u32_b32 v6, s20, 0
	v_mbcnt_hi_u32_b32 v6, s21, v6
	s_bcnt1_i32_b64 s16, s[20:21]
	v_cndmask_b32_e64 v4, v4, v6, s[20:21]
	v_writelane_b32 v5, s16, 8
	v_cmp_eq_u32_e64 s[20:21], 9, v2
	s_nop 1
	v_mbcnt_lo_u32_b32 v6, s20, 0
	v_mbcnt_hi_u32_b32 v6, s21, v6
	s_bcnt1_i32_b64 s16, s[20:21]
	v_cndmask_b32_e64 v4, v4, v6, s[20:21]
	v_writelane_b32 v5, s16, 9
	v_cmp_eq_u32_e64 s[20:21], 10, v2
	s_nop 1
	v_mbcnt_lo_u32_b32 v6, s20, 0
	v_mbcnt_hi_u32_b32 v6, s21, v6
	s_bcnt1_i32_b64 s16, s[20:21]
	v_cndmask_b32_e64 v4, v4, v6, s[20:21]
	v_writelane_b32 v5, s16, 10
	v_cmp_eq_u32_e64 s[20:21], 11, v2
	s_nop 1
	v_mbcnt_lo_u32_b32 v6, s20, 0
	v_mbcnt_hi_u32_b32 v6, s21, v6
	s_bcnt1_i32_b64 s16, s[20:21]
	v_cndmask_b32_e64 v4, v4, v6, s[20:21]
	v_writelane_b32 v5, s16, 11
	v_cmp_eq_u32_e64 s[20:21], 12, v2
	s_nop 1
	v_mbcnt_lo_u32_b32 v6, s20, 0
	v_mbcnt_hi_u32_b32 v6, s21, v6
	s_bcnt1_i32_b64 s16, s[20:21]
	v_cndmask_b32_e64 v4, v4, v6, s[20:21]
	v_writelane_b32 v5, s16, 12
	v_cmp_eq_u32_e64 s[20:21], 13, v2
	s_nop 1
	v_mbcnt_lo_u32_b32 v6, s20, 0
	v_mbcnt_hi_u32_b32 v6, s21, v6
	s_bcnt1_i32_b64 s16, s[20:21]
	v_cndmask_b32_e64 v4, v4, v6, s[20:21]
	v_writelane_b32 v5, s16, 13
	v_cmp_eq_u32_e64 s[20:21], 14, v2
	s_nop 1
	v_mbcnt_lo_u32_b32 v6, s20, 0
	v_mbcnt_hi_u32_b32 v6, s21, v6
	s_bcnt1_i32_b64 s16, s[20:21]
	v_cndmask_b32_e64 v4, v4, v6, s[20:21]
	v_writelane_b32 v5, s16, 14
	v_cmp_eq_u32_e64 s[20:21], 15, v2
	s_nop 1
	v_mbcnt_lo_u32_b32 v6, s20, 0
	v_mbcnt_hi_u32_b32 v6, s21, v6
	s_bcnt1_i32_b64 s16, s[20:21]
	v_cndmask_b32_e64 v4, v4, v6, s[20:21]
	v_writelane_b32 v5, s16, 15
	v_cmp_eq_u32_e64 s[20:21], 16, v2
	s_nop 1
	v_mbcnt_lo_u32_b32 v6, s20, 0
	v_mbcnt_hi_u32_b32 v6, s21, v6
	s_bcnt1_i32_b64 s16, s[20:21]
	v_cndmask_b32_e64 v4, v4, v6, s[20:21]
	v_writelane_b32 v5, s16, 16
; __global__ void __launch_bounds__(512, 2) hymba_fwd(Args args) {
;     ...
;                 for (int i = 0; i < 64; ++i) cnt += (selE[i] == e) ? 1 : 0;
;                 unsigned base = 0u;
;                 if (cnt) base = __hip_atomic_fetch_add((unsigned*)(ctl + CW_CNT + 64 * e), (unsigned)cnt, RLX_AGENT);
;                 for (int i = 0; i < 64; ++i) if (selE[i] == e) { const int t = t0 + (i >> 1); ltok[e * SEQ + base] = t; lw[e * SEQ + base] = selW[i]; tokpos[2 * t + (i & 1)] = (e << 16) | (int)base; ++base; }
	v_cmp_eq_u32_e64 s[20:21], 17, v2
	s_nop 1
	v_mbcnt_lo_u32_b32 v6, s20, 0
	v_mbcnt_hi_u32_b32 v6, s21, v6
	s_bcnt1_i32_b64 s16, s[20:21]
	v_cndmask_b32_e64 v4, v4, v6, s[20:21]
	v_writelane_b32 v5, s16, 17
	v_cmp_eq_u32_e64 s[20:21], 18, v2
	s_nop 1
	v_mbcnt_lo_u32_b32 v6, s20, 0
	v_mbcnt_hi_u32_b32 v6, s21, v6
	s_bcnt1_i32_b64 s16, s[20:21]
	v_cndmask_b32_e64 v4, v4, v6, s[20:21]
	v_writelane_b32 v5, s16, 18
	v_cmp_eq_u32_e64 s[20:21], 19, v2
	s_nop 1
	v_mbcnt_lo_u32_b32 v6, s20, 0
	v_mbcnt_hi_u32_b32 v6, s21, v6
	s_bcnt1_i32_b64 s16, s[20:21]
	v_cndmask_b32_e64 v4, v4, v6, s[20:21]
	v_writelane_b32 v5, s16, 19
	v_cmp_eq_u32_e64 s[20:21], 20, v2
	s_nop 1
	v_mbcnt_lo_u32_b32 v6, s20, 0
	v_mbcnt_hi_u32_b32 v6, s21, v6
	s_bcnt1_i32_b64 s16, s[20:21]
	v_cndmask_b32_e64 v4, v4, v6, s[20:21]
	v_writelane_b32 v5, s16, 20
	v_cmp_eq_u32_e64 s[20:21], 21, v2
	s_nop 1
	v_mbcnt_lo_u32_b32 v6, s20, 0
	v_mbcnt_hi_u32_b32 v6, s21, v6
	s_bcnt1_i32_b64 s16, s[20:21]
	v_cndmask_b32_e64 v4, v4, v6, s[20:21]
	v_writelane_b32 v5, s16, 21
	v_cmp_eq_u32_e64 s[20:21], 22, v2
	s_nop 1
	v_mbcnt_lo_u32_b32 v6, s20, 0
	v_mbcnt_hi_u32_b32 v6, s21, v6
	s_bcnt1_i32_b64 s16, s[20:21]
	v_cndmask_b32_e64 v4, v4, v6, s[20:21]
	v_writelane_b32 v5, s16, 22
	v_cmp_eq_u32_e64 s[20:21], 23, v2
	s_nop 1
	v_mbcnt_lo_u32_b32 v6, s20, 0
	v_mbcnt_hi_u32_b32 v6, s21, v6
	s_bcnt1_i32_b64 s16, s[20:21]
	v_cndmask_b32_e64 v4, v4, v6, s[20:21]
	v_writelane_b32 v5, s16, 23
	v_cmp_eq_u32_e64 s[20:21], 24, v2
	s_nop 1
	v_mbcnt_lo_u32_b32 v6, s20, 0
	v_mbcnt_hi_u32_b32 v6, s21, v6
	s_bcnt1_i32_b64 s16, s[20:21]
	v_cndmask_b32_e64 v4, v4, v6, s[20:21]
	v_writelane_b32 v5, s16, 24
	v_cmp_eq_u32_e64 s[20:21], 25, v2
	s_nop 1
	v_mbcnt_lo_u32_b32 v6, s20, 0
	v_mbcnt_hi_u32_b32 v6, s21, v6
	s_bcnt1_i32_b64 s16, s[20:21]
	v_cndmask_b32_e64 v4, v4, v6, s[20:21]
	v_writelane_b32 v5, s16, 25
	v_cmp_eq_u32_e64 s[20:21], 26, v2
	s_nop 1
	v_mbcnt_lo_u32_b32 v6, s20, 0
	v_mbcnt_hi_u32_b32 v6, s21, v6
	s_bcnt1_i32_b64 s16, s[20:21]
	v_cndmask_b32_e64 v4, v4, v6, s[20:21]
	v_writelane_b32 v5, s16, 26
	v_cmp_eq_u32_e64 s[20:21], 27, v2
	s_nop 1
	v_mbcnt_lo_u32_b32 v6, s20, 0
	v_mbcnt_hi_u32_b32 v6, s21, v6
	s_bcnt1_i32_b64 s16, s[20:21]
	v_cndmask_b32_e64 v4, v4, v6, s[20:21]
	v_writelane_b32 v5, s16, 27
	v_cmp_eq_u32_e64 s[20:21], 28, v2
	s_nop 1
	v_mbcnt_lo_u32_b32 v6, s20, 0
	v_mbcnt_hi_u32_b32 v6, s21, v6
	s_bcnt1_i32_b64 s16, s[20:21]
	v_cndmask_b32_e64 v4, v4, v6, s[20:21]
	v_writelane_b32 v5, s16, 28
	v_cmp_eq_u32_e64 s[20:21], 29, v2
	s_nop 1
	v_mbcnt_lo_u32_b32 v6, s20, 0
	v_mbcnt_hi_u32_b32 v6, s21, v6
	s_bcnt1_i32_b64 s16, s[20:21]
	v_cndmask_b32_e64 v4, v4, v6, s[20:21]
	v_writelane_b32 v5, s16, 29
	v_cmp_eq_u32_e64 s[20:21], 30, v2
	s_nop 1
	v_mbcnt_lo_u32_b32 v6, s20, 0
	v_mbcnt_hi_u32_b32 v6, s21, v6
	s_bcnt1_i32_b64 s16, s[20:21]
	v_cndmask_b32_e64 v4, v4, v6, s[20:21]
	v_writelane_b32 v5, s16, 30
	v_cmp_eq_u32_e64 s[20:21], 31, v2
	s_nop 1
	v_mbcnt_lo_u32_b32 v6, s20, 0
	v_mbcnt_hi_u32_b32 v6, s21, v6
	s_bcnt1_i32_b64 s16, s[20:21]
	v_cndmask_b32_e64 v4, v4, v6, s[20:21]
	v_writelane_b32 v5, s16, 31
	s_nop 1
	v_cmp_ne_u32_e32 vcc, 0, v5
	v_mov_b32_e32 v7, 0
	s_and_saveexec_b64 s[16:17], vcc
	global_atomic_add v7, v[166:167], v5, off sc0
	s_or_b64 exec, exec, s[16:17]
	s_waitcnt vmcnt(0)
	v_lshlrev_b32_e32 v8, 2, v2
	ds_bpermute_b32 v9, v8, v7
	v_lshrrev_b32_e32 v11, 1, v153
	v_add_u32_e32 v11, s56, v11
	s_lshl_b32 s16, s51, 2
	s_add_u32 s46, s48, s16
	s_addc_u32 s47, s49, 0
	v_lshlrev_b32_e32 v13, 2, v153
	s_waitcnt lgkmcnt(0)
	v_add_u32_e32 v9, v9, v4
	v_lshl_add_u32 v10, v2, 13, v9
	v_lshlrev_b32_e32 v10, 2, v10
	v_lshl_or_b32 v12, v2, 16, v9
	global_store_dword v10, v3, s[22:23]
	global_store_dword v10, v11, s[36:37]
	global_store_dword v13, v12, s[46:47]
	s_branch .LBB0_552
